# baseline (speedup 1.0000x reference)
.Lf1_LBB3_9:
	s_or_b64 exec, exec, s[16:17]
	s_add_i32 s16, s46, 2
	s_add_i32 s17, s46, 3
	s_cmp_eq_u32 s45, 0x3c04000
	s_cselect_b32 s47, s12, s41
	s_cselect_b32 s48, 0, s16
	s_cselect_b32 s49, s35, s42
	s_cselect_b32 s17, 1, s17
	s_add_i32 s50, s44, s45
	s_mov_b32 m0, s36
	s_nop 0
	buffer_load_dwordx4 v1, s[4:7], s50 offen lds
	s_mov_b32 m0, s37
	s_nop 0
	buffer_load_dwordx4 v204, s[4:7], s50 offen lds
	s_waitcnt lgkmcnt(0)
	s_waitcnt vmcnt(28)
	s_barrier
	s_setprio 1
	s_waitcnt lgkmcnt(0)
	v_mfma_f32_16x16x32_bf16 v[114:117], v[186:189], v[146:149], v[114:117]
	v_mfma_f32_16x16x32_bf16 v[110:113], v[186:189], v[154:157], v[110:113]
	v_mfma_f32_16x16x32_bf16 v[78:81], v[174:177], v[146:149], v[78:81]
	v_mfma_f32_16x16x32_bf16 v[74:77], v[174:177], v[154:157], v[74:77]
	v_mfma_f32_16x16x32_bf16 v[106:109], v[170:173], v[146:149], v[106:109]
	v_mfma_f32_16x16x32_bf16 v[102:105], v[170:173], v[154:157], v[102:105]
	v_mfma_f32_16x16x32_bf16 v[70:73], v[162:165], v[146:149], v[70:73]
	v_mfma_f32_16x16x32_bf16 v[66:69], v[162:165], v[154:157], v[66:69]
	v_mfma_f32_16x16x32_bf16 v[114:117], v[190:193], v[150:153], v[114:117]
	v_mfma_f32_16x16x32_bf16 v[110:113], v[190:193], v[158:161], v[110:113]
	v_mfma_f32_16x16x32_bf16 v[78:81], v[178:181], v[150:153], v[78:81]
	v_mfma_f32_16x16x32_bf16 v[74:77], v[178:181], v[158:161], v[74:77]
	v_mfma_f32_16x16x32_bf16 v[106:109], v[182:185], v[150:153], v[106:109]
	v_mfma_f32_16x16x32_bf16 v[102:105], v[182:185], v[158:161], v[102:105]
	v_mfma_f32_16x16x32_bf16 v[70:73], v[166:169], v[150:153], v[70:73]
	v_mfma_f32_16x16x32_bf16 v[66:69], v[166:169], v[158:161], v[66:69]
	s_setprio 0
	s_setprio 1
	v_mfma_f32_16x16x32_bf16 v[98:101], v[186:189], v[130:133], v[98:101]
	v_mfma_f32_16x16x32_bf16 v[18:21], v[186:189], v[138:141], v[18:21]
	v_mfma_f32_16x16x32_bf16 v[62:65], v[174:177], v[130:133], v[62:65]
	v_mfma_f32_16x16x32_bf16 v[2:5], v[174:177], v[138:141], v[2:5]
	v_mfma_f32_16x16x32_bf16 v[94:97], v[170:173], v[130:133], v[94:97]
	v_mfma_f32_16x16x32_bf16 v[26:29], v[170:173], v[138:141], v[26:29]
	v_mfma_f32_16x16x32_bf16 v[54:57], v[162:165], v[130:133], v[54:57]
	v_mfma_f32_16x16x32_bf16 v[10:13], v[162:165], v[138:141], v[10:13]
	v_mfma_f32_16x16x32_bf16 v[98:101], v[190:193], v[134:137], v[98:101]
	v_mfma_f32_16x16x32_bf16 v[18:21], v[190:193], v[142:145], v[18:21]
	v_mfma_f32_16x16x32_bf16 v[62:65], v[178:181], v[134:137], v[62:65]
	v_mfma_f32_16x16x32_bf16 v[2:5], v[178:181], v[142:145], v[2:5]
	v_mfma_f32_16x16x32_bf16 v[94:97], v[182:185], v[134:137], v[94:97]
	v_mfma_f32_16x16x32_bf16 v[26:29], v[182:185], v[142:145], v[26:29]
	v_mfma_f32_16x16x32_bf16 v[54:57], v[166:169], v[134:137], v[54:57]
	v_mfma_f32_16x16x32_bf16 v[10:13], v[166:169], v[142:145], v[10:13]
	s_setprio 0
	s_barrier
	s_lshl_b32 s49, s49, 6
	s_lshl_b32 s50, s48, 18
	s_or_b32 s51, s49, s50
	s_mov_b32 m0, s21
	s_lshl_b32 s51, s51, 1
	ds_read_b128 v[162:165], v226 offset:16384
	ds_read_b128 v[166:169], v226 offset:18432
	ds_read_b128 v[170:173], v227 offset:16384
	ds_read_b128 v[174:177], v227 offset:18432
	ds_read_b128 v[178:181], v226 offset:20480
	ds_read_b128 v[182:185], v226 offset:22528
	ds_read_b128 v[186:189], v227 offset:20480
	ds_read_b128 v[190:193], v227 offset:22528
	buffer_load_dwordx4 v199, s[8:11], s51 offen lds
	s_mov_b32 m0, s22
	s_lshl_b32 s48, s48, 22
	buffer_load_dwordx4 v205, s[8:11], s51 offen lds
	s_or_b32 s51, s49, 0x2000
	s_or_b32 s50, s51, s50
	s_lshl_b32 s50, s50, 1
	s_mov_b32 m0, s23
	s_lshl_b32 s47, s47, 7
	buffer_load_dwordx4 v199, s[8:11], s50 offen lds
	s_mov_b32 m0, s24
	s_add_i32 s48, s47, s48
	buffer_load_dwordx4 v205, s[8:11], s50 offen lds
	s_mov_b32 m0, s20
	s_nop 0
	buffer_load_dwordx4 v1, s[4:7], s48 offen lds
	s_mov_b32 m0, s25
	s_nop 0
	buffer_load_dwordx4 v204, s[4:7], s48 offen lds
	s_waitcnt lgkmcnt(0)
	s_waitcnt vmcnt(28)
	s_barrier
	s_setprio 1
	s_waitcnt lgkmcnt(0)
	v_mfma_f32_16x16x32_bf16 v[90:93], v[162:165], v[146:149], v[90:93]
	v_mfma_f32_16x16x32_bf16 v[86:89], v[162:165], v[154:157], v[86:89]
	v_mfma_f32_16x16x32_bf16 v[42:45], v[166:169], v[146:149], v[42:45]
	v_mfma_f32_16x16x32_bf16 v[38:41], v[166:169], v[154:157], v[38:41]
	v_mfma_f32_16x16x32_bf16 v[126:129], v[178:181], v[146:149], v[126:129]
	v_mfma_f32_16x16x32_bf16 v[122:125], v[178:181], v[154:157], v[122:125]
	v_mfma_f32_16x16x32_bf16 v[58:61], v[182:185], v[146:149], v[58:61]
	v_mfma_f32_16x16x32_bf16 v[50:53], v[182:185], v[154:157], v[50:53]
	v_mfma_f32_16x16x32_bf16 v[90:93], v[170:173], v[150:153], v[90:93]
	v_mfma_f32_16x16x32_bf16 v[86:89], v[170:173], v[158:161], v[86:89]
	v_mfma_f32_16x16x32_bf16 v[42:45], v[174:177], v[150:153], v[42:45]
	v_mfma_f32_16x16x32_bf16 v[38:41], v[174:177], v[158:161], v[38:41]
	v_mfma_f32_16x16x32_bf16 v[126:129], v[186:189], v[150:153], v[126:129]
	v_mfma_f32_16x16x32_bf16 v[122:125], v[186:189], v[158:161], v[122:125]
	v_mfma_f32_16x16x32_bf16 v[58:61], v[190:193], v[150:153], v[58:61]
	v_mfma_f32_16x16x32_bf16 v[50:53], v[190:193], v[158:161], v[50:53]
	s_setprio 0
	s_setprio 1
	v_mfma_f32_16x16x32_bf16 v[82:85], v[162:165], v[130:133], v[82:85]
	v_mfma_f32_16x16x32_bf16 v[22:25], v[162:165], v[138:141], v[22:25]
	v_mfma_f32_16x16x32_bf16 v[34:37], v[166:169], v[130:133], v[34:37]
	v_mfma_f32_16x16x32_bf16 v[6:9], v[166:169], v[138:141], v[6:9]
	v_mfma_f32_16x16x32_bf16 v[118:121], v[178:181], v[130:133], v[118:121]
	v_mfma_f32_16x16x32_bf16 v[30:33], v[178:181], v[138:141], v[30:33]
	v_mfma_f32_16x16x32_bf16 v[46:49], v[182:185], v[130:133], v[46:49]
	v_mfma_f32_16x16x32_bf16 v[14:17], v[182:185], v[138:141], v[14:17]
	v_mfma_f32_16x16x32_bf16 v[82:85], v[170:173], v[134:137], v[82:85]
	v_mfma_f32_16x16x32_bf16 v[22:25], v[170:173], v[142:145], v[22:25]
	v_mfma_f32_16x16x32_bf16 v[34:37], v[174:177], v[134:137], v[34:37]
	v_mfma_f32_16x16x32_bf16 v[6:9], v[174:177], v[142:145], v[6:9]
	v_mfma_f32_16x16x32_bf16 v[118:121], v[186:189], v[134:137], v[118:121]
	v_mfma_f32_16x16x32_bf16 v[30:33], v[186:189], v[142:145], v[30:33]
	v_mfma_f32_16x16x32_bf16 v[46:49], v[190:193], v[134:137], v[46:49]
	v_mfma_f32_16x16x32_bf16 v[14:17], v[190:193], v[142:145], v[14:17]
	s_setprio 0
	s_barrier
	s_branch .Lg1_loop_p3

.Lg1_loop_p3:
	v_add_u32_e32 v130, v218, v211
	v_add_u32_e32 v134, v218, v213
	v_add_u32_e32 v138, v219, v211
	v_add_u32_e32 v142, v219, v213
	v_add_u32_e32 v146, v220, v211
	v_add_u32_e32 v150, v220, v213
	v_add_u32_e32 v154, v221, v211
	v_add_u32_e32 v158, v221, v213
	s_addk_i32 s48, 0x4000
	s_mov_b32 m0, s26
	ds_read_b128 v[130:133], v130
	ds_read_b128 v[134:137], v134
	ds_read_b128 v[138:141], v138
	ds_read_b128 v[142:145], v142
	ds_read_b128 v[146:149], v146
	ds_read_b128 v[150:153], v150
	ds_read_b128 v[154:157], v154
	ds_read_b128 v[158:161], v158
	ds_read_b128 v[162:165], v226 offset:32768
	ds_read_b128 v[166:169], v226 offset:34816
	ds_read_b128 v[170:173], v227 offset:32768
	ds_read_b128 v[174:177], v227 offset:34816
	ds_read_b128 v[178:181], v226 offset:36864
	ds_read_b128 v[182:185], v226 offset:38912
	ds_read_b128 v[186:189], v227 offset:36864
	ds_read_b128 v[190:193], v227 offset:38912
	buffer_load_dwordx4 v1, s[4:7], s48 offen lds
	s_mov_b32 m0, s27
	s_nop 0
	buffer_load_dwordx4 v204, s[4:7], s48 offen lds
	s_waitcnt lgkmcnt(0)
	s_waitcnt vmcnt(8)
	s_barrier
	s_setprio 1
	s_waitcnt lgkmcnt(0)
	v_mfma_f32_16x16x32_bf16 v[114:117], v[162:165], v[130:133], v[114:117]
	v_mfma_f32_16x16x32_bf16 v[110:113], v[162:165], v[138:141], v[110:113]
	v_mfma_f32_16x16x32_bf16 v[78:81], v[166:169], v[130:133], v[78:81]
	v_mfma_f32_16x16x32_bf16 v[74:77], v[166:169], v[138:141], v[74:77]
	v_mfma_f32_16x16x32_bf16 v[106:109], v[178:181], v[130:133], v[106:109]
	v_mfma_f32_16x16x32_bf16 v[102:105], v[178:181], v[138:141], v[102:105]
	v_mfma_f32_16x16x32_bf16 v[70:73], v[182:185], v[130:133], v[70:73]
	v_mfma_f32_16x16x32_bf16 v[66:69], v[182:185], v[138:141], v[66:69]
	v_mfma_f32_16x16x32_bf16 v[114:117], v[170:173], v[134:137], v[114:117]
	v_mfma_f32_16x16x32_bf16 v[110:113], v[170:173], v[142:145], v[110:113]
	v_mfma_f32_16x16x32_bf16 v[78:81], v[174:177], v[134:137], v[78:81]
	v_mfma_f32_16x16x32_bf16 v[74:77], v[174:177], v[142:145], v[74:77]
	v_mfma_f32_16x16x32_bf16 v[106:109], v[186:189], v[134:137], v[106:109]
	v_mfma_f32_16x16x32_bf16 v[102:105], v[186:189], v[142:145], v[102:105]
	v_mfma_f32_16x16x32_bf16 v[70:73], v[190:193], v[134:137], v[70:73]
	v_mfma_f32_16x16x32_bf16 v[66:69], v[190:193], v[142:145], v[66:69]
	s_setprio 0
	s_setprio 1
	v_mfma_f32_16x16x32_bf16 v[98:101], v[162:165], v[146:149], v[98:101]
	v_mfma_f32_16x16x32_bf16 v[18:21], v[162:165], v[154:157], v[18:21]
	v_mfma_f32_16x16x32_bf16 v[62:65], v[166:169], v[146:149], v[62:65]
	v_mfma_f32_16x16x32_bf16 v[2:5], v[166:169], v[154:157], v[2:5]
	v_mfma_f32_16x16x32_bf16 v[94:97], v[178:181], v[146:149], v[94:97]
	v_mfma_f32_16x16x32_bf16 v[26:29], v[178:181], v[154:157], v[26:29]
	v_mfma_f32_16x16x32_bf16 v[54:57], v[182:185], v[146:149], v[54:57]
	v_mfma_f32_16x16x32_bf16 v[10:13], v[182:185], v[154:157], v[10:13]
	v_mfma_f32_16x16x32_bf16 v[98:101], v[170:173], v[150:153], v[98:101]
	v_mfma_f32_16x16x32_bf16 v[18:21], v[170:173], v[158:161], v[18:21]
	v_mfma_f32_16x16x32_bf16 v[62:65], v[174:177], v[150:153], v[62:65]
	v_mfma_f32_16x16x32_bf16 v[2:5], v[174:177], v[158:161], v[2:5]
	v_mfma_f32_16x16x32_bf16 v[94:97], v[186:189], v[150:153], v[94:97]
	v_mfma_f32_16x16x32_bf16 v[26:29], v[186:189], v[158:161], v[26:29]
	v_mfma_f32_16x16x32_bf16 v[54:57], v[190:193], v[150:153], v[54:57]
	v_mfma_f32_16x16x32_bf16 v[10:13], v[190:193], v[158:161], v[10:13]
	s_setprio 0
	s_barrier
	s_cmp_gt_u32 s46, 13
	s_cbranch_scc1 .Lp4_last
	s_lshl_b32 s48, s17, 18
	s_or_b32 s49, s49, s48
	s_mov_b32 m0, s28
	s_lshl_b32 s49, s49, 1
	ds_read_b128 v[162:165], v226 offset:49152
	ds_read_b128 v[166:169], v226 offset:51200
	ds_read_b128 v[170:173], v227 offset:49152
	ds_read_b128 v[174:177], v227 offset:51200
	ds_read_b128 v[178:181], v226 offset:53248
	ds_read_b128 v[182:185], v226 offset:55296
	ds_read_b128 v[186:189], v227 offset:53248
	ds_read_b128 v[190:193], v227 offset:55296
	buffer_load_dwordx4 v199, s[8:11], s49 offen lds
	s_mov_b32 m0, s29
	s_or_b32 s48, s51, s48
	buffer_load_dwordx4 v205, s[8:11], s49 offen lds
	s_lshl_b32 s48, s48, 1
	s_mov_b32 m0, s30
	s_lshl_b32 s17, s17, 22
	buffer_load_dwordx4 v199, s[8:11], s48 offen lds
	s_mov_b32 m0, s31
	s_add_i32 s17, s17, s47
	buffer_load_dwordx4 v205, s[8:11], s48 offen lds
	s_mov_b32 m0, s33
	s_nop 0
	buffer_load_dwordx4 v1, s[4:7], s17 offen lds
	s_mov_b32 m0, s34
	s_nop 0
	buffer_load_dwordx4 v204, s[4:7], s17 offen lds
	s_waitcnt lgkmcnt(0)
	s_waitcnt vmcnt(8)
	s_barrier
	s_setprio 1
	s_waitcnt lgkmcnt(0)
	v_mfma_f32_16x16x32_bf16 v[90:93], v[162:165], v[130:133], v[90:93]
	v_mfma_f32_16x16x32_bf16 v[86:89], v[162:165], v[138:141], v[86:89]
	v_mfma_f32_16x16x32_bf16 v[42:45], v[166:169], v[130:133], v[42:45]
	v_mfma_f32_16x16x32_bf16 v[38:41], v[166:169], v[138:141], v[38:41]
	v_mfma_f32_16x16x32_bf16 v[126:129], v[178:181], v[130:133], v[126:129]
	v_mfma_f32_16x16x32_bf16 v[122:125], v[178:181], v[138:141], v[122:125]
	v_mfma_f32_16x16x32_bf16 v[58:61], v[182:185], v[130:133], v[58:61]
	v_mfma_f32_16x16x32_bf16 v[50:53], v[182:185], v[138:141], v[50:53]
	v_mfma_f32_16x16x32_bf16 v[90:93], v[170:173], v[134:137], v[90:93]
	v_mfma_f32_16x16x32_bf16 v[86:89], v[170:173], v[142:145], v[86:89]
	v_mfma_f32_16x16x32_bf16 v[42:45], v[174:177], v[134:137], v[42:45]
	v_mfma_f32_16x16x32_bf16 v[38:41], v[174:177], v[142:145], v[38:41]
	v_mfma_f32_16x16x32_bf16 v[126:129], v[186:189], v[134:137], v[126:129]
	v_mfma_f32_16x16x32_bf16 v[122:125], v[186:189], v[142:145], v[122:125]
	v_mfma_f32_16x16x32_bf16 v[58:61], v[190:193], v[134:137], v[58:61]
	v_mfma_f32_16x16x32_bf16 v[50:53], v[190:193], v[142:145], v[50:53]
	s_setprio 0
	s_setprio 1
	v_mfma_f32_16x16x32_bf16 v[82:85], v[162:165], v[146:149], v[82:85]
	v_mfma_f32_16x16x32_bf16 v[22:25], v[162:165], v[154:157], v[22:25]
	v_mfma_f32_16x16x32_bf16 v[34:37], v[166:169], v[146:149], v[34:37]
	v_mfma_f32_16x16x32_bf16 v[6:9], v[166:169], v[154:157], v[6:9]
	v_mfma_f32_16x16x32_bf16 v[118:121], v[178:181], v[146:149], v[118:121]
	v_mfma_f32_16x16x32_bf16 v[30:33], v[178:181], v[154:157], v[30:33]
	v_mfma_f32_16x16x32_bf16 v[46:49], v[182:185], v[146:149], v[46:49]
	v_mfma_f32_16x16x32_bf16 v[14:17], v[182:185], v[154:157], v[14:17]
	v_mfma_f32_16x16x32_bf16 v[82:85], v[170:173], v[150:153], v[82:85]
	v_mfma_f32_16x16x32_bf16 v[22:25], v[170:173], v[158:161], v[22:25]
	v_mfma_f32_16x16x32_bf16 v[34:37], v[174:177], v[150:153], v[34:37]
	v_mfma_f32_16x16x32_bf16 v[6:9], v[174:177], v[158:161], v[6:9]
	v_mfma_f32_16x16x32_bf16 v[118:121], v[186:189], v[150:153], v[118:121]
	v_mfma_f32_16x16x32_bf16 v[30:33], v[186:189], v[158:161], v[30:33]
	v_mfma_f32_16x16x32_bf16 v[46:49], v[190:193], v[150:153], v[46:49]
	v_mfma_f32_16x16x32_bf16 v[14:17], v[190:193], v[158:161], v[14:17]
	s_setprio 0
	s_barrier
	s_add_i32 s45, s45, 0x800000
	s_mov_b32 s46, s16
	s_branch .LBB3_7
